# speedup vs baseline: 1.0136x; 1.0136x over previous
.Lk1_nowarm9:
	buffer_load_dword v8, v1, s[8:11], s40 offen nt
	buffer_load_dword v9, v1, s[8:11], s41 offen nt
	buffer_load_dword v10, v1, s[8:11], s42 offen nt
	buffer_load_dword v11, v1, s[8:11], s43 offen nt
	buffer_load_dword v12, v1, s[8:11], s44 offen nt
	buffer_load_dword v13, v1, s[8:11], s45 offen nt
	buffer_load_dword v14, v1, s[8:11], s46 offen nt
	buffer_load_dword v15, v1, s[8:11], s47 offen nt
	buffer_load_dword v16, v1, s[8:11], s48 offen nt
	buffer_load_dword v17, v1, s[8:11], s49 offen nt
	buffer_load_dword v18, v1, s[8:11], s50 offen nt
	buffer_load_dword v19, v1, s[8:11], s51 offen nt
	buffer_load_dword v20, v1, s[8:11], s52 offen nt
	buffer_load_dword v21, v1, s[8:11], s53 offen nt
	buffer_load_dword v22, v1, s[8:11], s54 offen nt
	buffer_load_dword v23, v1, s[8:11], s55 offen nt
	s_add_u32 s8, s8, 0x4e200
	s_addc_u32 s9, s9, 0
	buffer_load_dword v24, v1, s[8:11], s40 offen nt
	buffer_load_dword v25, v1, s[8:11], s41 offen nt
	buffer_load_dword v26, v1, s[8:11], s42 offen nt
	buffer_load_dword v27, v1, s[8:11], s43 offen nt
	buffer_load_dword v28, v1, s[8:11], s44 offen nt
	buffer_load_dword v29, v1, s[8:11], s45 offen nt
	buffer_load_dword v30, v1, s[8:11], s46 offen nt
	buffer_load_dword v31, v1, s[8:11], s47 offen nt
	buffer_load_dword v32, v1, s[8:11], s48 offen nt
	buffer_load_dword v33, v1, s[8:11], s49 offen nt
	buffer_load_dword v34, v1, s[8:11], s50 offen nt
	buffer_load_dword v35, v1, s[8:11], s51 offen nt
	buffer_load_dword v36, v1, s[8:11], s52 offen nt
	buffer_load_dword v37, v1, s[8:11], s53 offen nt
	buffer_load_dword v38, v1, s[8:11], s54 offen nt
	buffer_load_dword v39, v1, s[8:11], s55 offen nt
	s_add_u32 s8, s8, 0x4e200
	s_addc_u32 s9, s9, 0
	buffer_load_dword v40, v1, s[8:11], s40 offen nt
	buffer_load_dword v41, v1, s[8:11], s41 offen nt
	buffer_load_dword v42, v1, s[8:11], s42 offen nt
	buffer_load_dword v43, v1, s[8:11], s43 offen nt
	buffer_load_dword v44, v1, s[8:11], s44 offen nt
	buffer_load_dword v45, v1, s[8:11], s45 offen nt
	buffer_load_dword v46, v1, s[8:11], s46 offen nt
	buffer_load_dword v47, v1, s[8:11], s47 offen nt
	buffer_load_dword v48, v1, s[8:11], s48 offen nt
	buffer_load_dword v49, v1, s[8:11], s49 offen nt
	buffer_load_dword v50, v1, s[8:11], s50 offen nt
	buffer_load_dword v51, v1, s[8:11], s51 offen nt
	buffer_load_dword v52, v1, s[8:11], s52 offen nt
	buffer_load_dword v53, v1, s[8:11], s53 offen nt
	buffer_load_dword v54, v1, s[8:11], s54 offen nt
	buffer_load_dword v55, v1, s[8:11], s55 offen nt
	s_add_u32 s8, s8, 0x4e200
	s_addc_u32 s9, s9, 0
	buffer_load_dword v56, v1, s[8:11], s40 offen nt
	buffer_load_dword v57, v1, s[8:11], s41 offen nt
	buffer_load_dword v58, v1, s[8:11], s42 offen nt
	buffer_load_dword v59, v1, s[8:11], s43 offen nt
	buffer_load_dword v60, v1, s[8:11], s44 offen nt
	buffer_load_dword v61, v1, s[8:11], s45 offen nt
	buffer_load_dword v62, v1, s[8:11], s46 offen nt
	buffer_load_dword v63, v1, s[8:11], s47 offen nt
	buffer_load_dword v64, v1, s[8:11], s48 offen nt
	buffer_load_dword v65, v1, s[8:11], s49 offen nt
	buffer_load_dword v66, v1, s[8:11], s50 offen nt
	v_mul_u32_u24_e32 v3, 0x147b, v2
	v_lshrrev_b32_e32 v3, 19, v3
	v_mul_u32_u24_e32 v98, 0x64, v3
	v_sub_u32_e32 v98, v2, v98
	v_add_u32_e32 v3, -1, v3
	v_add_u32_e32 v98, -1, v98
	s_movk_i32 s17, 0x62
	v_cmp_gt_u32_e64 s[36:37], 48, v3
	v_cmp_gt_u32_e64 s[38:39], s17, v98
	s_mul_i32 s17, s15, 0x1388
	v_add_lshl_u32 v98, v2, s17, 3
	s_and_b64 s[36:37], s[36:37], s[38:39]
	s_waitcnt vmcnt(55)
	buffer_load_dword v67, v1, s[8:11], s51 offen nt
	buffer_load_dword v68, v1, s[8:11], s52 offen nt
	buffer_load_dword v69, v1, s[8:11], s53 offen nt
	buffer_load_dword v70, v1, s[8:11], s54 offen nt
	buffer_load_dword v71, v1, s[8:11], s55 offen nt
	s_add_u32 s8, s8, 0x4e200
	s_addc_u32 s9, s9, 0
	buffer_load_dword v72, v1, s[8:11], s40 offen nt
	s_waitcnt vmcnt(49)
	v_max3_f32 v76, v8, v9, v10
	v_max3_f32 v76, v76, v11, v12
	v_max3_f32 v76, v76, v13, v14
	v_max3_f32 v76, v76, v15, v16
	v_max3_f32 v76, v76, v17, v18
	v_max3_f32 v76, v76, v19, v20
	v_max3_f32 v76, v76, v21, v22
	v_max_f32_e32 v76, v76, v23
	v_pk_add_f32 v[8:9], v[8:9], v[76:77] op_sel_hi:[1,0] neg_lo:[0,1] neg_hi:[0,1]
	v_pk_add_f32 v[10:11], v[10:11], v[76:77] op_sel_hi:[1,0] neg_lo:[0,1] neg_hi:[0,1]
	v_pk_add_f32 v[12:13], v[12:13], v[76:77] op_sel_hi:[1,0] neg_lo:[0,1] neg_hi:[0,1]
	v_pk_add_f32 v[14:15], v[14:15], v[76:77] op_sel_hi:[1,0] neg_lo:[0,1] neg_hi:[0,1]
	v_pk_add_f32 v[16:17], v[16:17], v[76:77] op_sel_hi:[1,0] neg_lo:[0,1] neg_hi:[0,1]
	v_pk_add_f32 v[18:19], v[18:19], v[76:77] op_sel_hi:[1,0] neg_lo:[0,1] neg_hi:[0,1]
	v_pk_add_f32 v[20:21], v[20:21], v[76:77] op_sel_hi:[1,0] neg_lo:[0,1] neg_hi:[0,1]
	v_pk_add_f32 v[22:23], v[22:23], v[76:77] op_sel_hi:[1,0] neg_lo:[0,1] neg_hi:[0,1]
	v_or_b32_e32 v81, 0, v8
	v_or_b32_e32 v82, 1, v9
	v_min_u32_e32 v80, v81, v82
	v_or_b32_e32 v81, 2, v10
	v_or_b32_e32 v82, 3, v11
	v_min3_u32 v80, v80, v81, v82
	v_or_b32_e32 v81, 4, v12
	v_or_b32_e32 v82, 5, v13
	v_min3_u32 v80, v80, v81, v82
	v_or_b32_e32 v81, 6, v14
	v_or_b32_e32 v82, 7, v15
	v_min3_u32 v80, v80, v81, v82
	v_or_b32_e32 v81, 8, v16
	v_or_b32_e32 v82, 9, v17
	v_min3_u32 v80, v80, v81, v82
	v_or_b32_e32 v81, 10, v18
	v_or_b32_e32 v82, 11, v19
	v_min3_u32 v80, v80, v81, v82
	v_or_b32_e32 v81, 12, v20
	v_or_b32_e32 v82, 13, v21
	v_min3_u32 v80, v80, v81, v82
	v_or_b32_e32 v81, 14, v22
	v_or_b32_e32 v82, 15, v23
	v_min3_u32 v80, v80, v81, v82
	v_pk_mul_f32 v[8:9], v[8:9], s[14:15] op_sel_hi:[1,0]
	v_pk_mul_f32 v[10:11], v[10:11], s[14:15] op_sel_hi:[1,0]
	v_pk_mul_f32 v[12:13], v[12:13], s[14:15] op_sel_hi:[1,0]
	v_pk_mul_f32 v[14:15], v[14:15], s[14:15] op_sel_hi:[1,0]
	v_pk_mul_f32 v[16:17], v[16:17], s[14:15] op_sel_hi:[1,0]
	v_pk_mul_f32 v[18:19], v[18:19], s[14:15] op_sel_hi:[1,0]
	v_pk_mul_f32 v[20:21], v[20:21], s[14:15] op_sel_hi:[1,0]
	v_pk_mul_f32 v[22:23], v[22:23], s[14:15] op_sel_hi:[1,0]
	v_exp_f32_e32 v8, v8
	v_exp_f32_e32 v9, v9
	v_exp_f32_e32 v10, v10
	v_exp_f32_e32 v11, v11
	v_exp_f32_e32 v12, v12
	v_exp_f32_e32 v13, v13
	v_exp_f32_e32 v14, v14
	v_exp_f32_e32 v15, v15
	v_exp_f32_e32 v16, v16
	v_exp_f32_e32 v17, v17
	v_exp_f32_e32 v18, v18
	v_exp_f32_e32 v19, v19
	v_exp_f32_e32 v20, v20
	v_exp_f32_e32 v21, v21
	v_exp_f32_e32 v22, v22
	v_exp_f32_e32 v23, v23
	v_pk_add_f32 v[78:79], v[8:9], v[10:11]
	v_pk_add_f32 v[78:79], v[78:79], v[12:13]
	v_pk_add_f32 v[78:79], v[78:79], v[14:15]
	v_pk_add_f32 v[78:79], v[78:79], v[16:17]
	v_pk_add_f32 v[78:79], v[78:79], v[18:19]
	v_pk_add_f32 v[78:79], v[78:79], v[20:21]
	v_pk_add_f32 v[78:79], v[78:79], v[22:23]
	v_add_f32_e32 v78, v78, v79
	v_cvt_f64_f32_e32 v[86:87], v78
	v_mov_b32_e32 v75, v80
	v_mov_b32_e32 v73, v76
	s_waitcnt vmcnt(33)
	v_max3_f32 v76, v24, v25, v26
	v_max3_f32 v76, v76, v27, v28
	v_max3_f32 v76, v76, v29, v30
	v_max3_f32 v76, v76, v31, v32
	v_max3_f32 v76, v76, v33, v34
	v_max3_f32 v76, v76, v35, v36
	v_max3_f32 v76, v76, v37, v38
	v_max_f32_e32 v76, v76, v39
	v_max_f32_e32 v100, v73, v76
	v_cmp_gt_f32_e64 s[26:27], v76, v73
	v_sub_f32_e32 v83, v73, v100
	v_mul_f32_e32 v83, s14, v83
	v_exp_f32_e32 v83, v83
	v_pk_add_f32 v[24:25], v[24:25], v[100:101] op_sel_hi:[1,0] neg_lo:[0,1] neg_hi:[0,1]
	v_pk_add_f32 v[26:27], v[26:27], v[100:101] op_sel_hi:[1,0] neg_lo:[0,1] neg_hi:[0,1]
	v_pk_add_f32 v[28:29], v[28:29], v[100:101] op_sel_hi:[1,0] neg_lo:[0,1] neg_hi:[0,1]
	v_pk_add_f32 v[30:31], v[30:31], v[100:101] op_sel_hi:[1,0] neg_lo:[0,1] neg_hi:[0,1]
	v_pk_add_f32 v[32:33], v[32:33], v[100:101] op_sel_hi:[1,0] neg_lo:[0,1] neg_hi:[0,1]
	v_pk_add_f32 v[34:35], v[34:35], v[100:101] op_sel_hi:[1,0] neg_lo:[0,1] neg_hi:[0,1]
	v_pk_add_f32 v[36:37], v[36:37], v[100:101] op_sel_hi:[1,0] neg_lo:[0,1] neg_hi:[0,1]
	v_pk_add_f32 v[38:39], v[38:39], v[100:101] op_sel_hi:[1,0] neg_lo:[0,1] neg_hi:[0,1]
	v_cvt_f64_f32_e32 v[84:85], v83
	v_or_b32_e32 v81, 16, v24
	v_or_b32_e32 v82, 17, v25
	v_min_u32_e32 v80, v81, v82
	v_or_b32_e32 v81, 18, v26
	v_or_b32_e32 v82, 19, v27
	v_min3_u32 v80, v80, v81, v82
	v_or_b32_e32 v81, 20, v28
	v_or_b32_e32 v82, 21, v29
	v_min3_u32 v80, v80, v81, v82
	v_or_b32_e32 v81, 22, v30
	v_or_b32_e32 v82, 23, v31
	v_min3_u32 v80, v80, v81, v82
	v_or_b32_e32 v81, 24, v32
	v_or_b32_e32 v82, 25, v33
	v_min3_u32 v80, v80, v81, v82
	v_or_b32_e32 v81, 26, v34
	v_or_b32_e32 v82, 27, v35
	v_min3_u32 v80, v80, v81, v82
	v_or_b32_e32 v81, 28, v36
	v_or_b32_e32 v82, 29, v37
	v_min3_u32 v80, v80, v81, v82
	v_or_b32_e32 v81, 30, v38
	v_or_b32_e32 v82, 31, v39
	v_min3_u32 v80, v80, v81, v82
	v_mul_f64 v[86:87], v[86:87], v[84:85]
	v_pk_mul_f32 v[24:25], v[24:25], s[14:15] op_sel_hi:[1,0]
	v_pk_mul_f32 v[26:27], v[26:27], s[14:15] op_sel_hi:[1,0]
	v_pk_mul_f32 v[28:29], v[28:29], s[14:15] op_sel_hi:[1,0]
	v_pk_mul_f32 v[30:31], v[30:31], s[14:15] op_sel_hi:[1,0]
	v_pk_mul_f32 v[32:33], v[32:33], s[14:15] op_sel_hi:[1,0]
	v_pk_mul_f32 v[34:35], v[34:35], s[14:15] op_sel_hi:[1,0]
	v_pk_mul_f32 v[36:37], v[36:37], s[14:15] op_sel_hi:[1,0]
	v_pk_mul_f32 v[38:39], v[38:39], s[14:15] op_sel_hi:[1,0]
	v_exp_f32_e32 v24, v24
	v_exp_f32_e32 v25, v25
	v_exp_f32_e32 v26, v26
	v_exp_f32_e32 v27, v27
	v_exp_f32_e32 v28, v28
	v_exp_f32_e32 v29, v29
	v_exp_f32_e32 v30, v30
	v_exp_f32_e32 v31, v31
	v_exp_f32_e32 v32, v32
	v_exp_f32_e32 v33, v33
	v_exp_f32_e32 v34, v34
	v_exp_f32_e32 v35, v35
	v_exp_f32_e32 v36, v36
	v_exp_f32_e32 v37, v37
	v_exp_f32_e32 v38, v38
	v_exp_f32_e32 v39, v39
	v_pk_add_f32 v[78:79], v[24:25], v[26:27]
	v_pk_add_f32 v[78:79], v[78:79], v[28:29]
	v_pk_add_f32 v[78:79], v[78:79], v[30:31]
	v_pk_add_f32 v[78:79], v[78:79], v[32:33]
	v_pk_add_f32 v[78:79], v[78:79], v[34:35]
	v_pk_add_f32 v[78:79], v[78:79], v[36:37]
	v_pk_add_f32 v[78:79], v[78:79], v[38:39]
	v_add_f32_e32 v78, v78, v79
	v_cvt_f64_f32_e32 v[84:85], v78
	v_cndmask_b32_e64 v75, v75, v80, s[26:27]
	v_mov_b32_e32 v73, v100
	v_add_f64 v[86:87], v[86:87], v[84:85]
	s_waitcnt vmcnt(17)
	v_max3_f32 v76, v40, v41, v42
	v_max3_f32 v76, v76, v43, v44
	v_max3_f32 v76, v76, v45, v46
	v_max3_f32 v76, v76, v47, v48
	v_max3_f32 v76, v76, v49, v50
	v_max3_f32 v76, v76, v51, v52
	v_max3_f32 v76, v76, v53, v54
	v_max_f32_e32 v76, v76, v55
	v_max_f32_e32 v100, v73, v76
	v_cmp_gt_f32_e64 s[26:27], v76, v73
	v_sub_f32_e32 v83, v73, v100
	v_mul_f32_e32 v83, s14, v83
	v_exp_f32_e32 v83, v83
	v_pk_add_f32 v[40:41], v[40:41], v[100:101] op_sel_hi:[1,0] neg_lo:[0,1] neg_hi:[0,1]
	v_pk_add_f32 v[42:43], v[42:43], v[100:101] op_sel_hi:[1,0] neg_lo:[0,1] neg_hi:[0,1]
	v_pk_add_f32 v[44:45], v[44:45], v[100:101] op_sel_hi:[1,0] neg_lo:[0,1] neg_hi:[0,1]
	v_pk_add_f32 v[46:47], v[46:47], v[100:101] op_sel_hi:[1,0] neg_lo:[0,1] neg_hi:[0,1]
	v_pk_add_f32 v[48:49], v[48:49], v[100:101] op_sel_hi:[1,0] neg_lo:[0,1] neg_hi:[0,1]
	v_pk_add_f32 v[50:51], v[50:51], v[100:101] op_sel_hi:[1,0] neg_lo:[0,1] neg_hi:[0,1]
	v_pk_add_f32 v[52:53], v[52:53], v[100:101] op_sel_hi:[1,0] neg_lo:[0,1] neg_hi:[0,1]
	v_pk_add_f32 v[54:55], v[54:55], v[100:101] op_sel_hi:[1,0] neg_lo:[0,1] neg_hi:[0,1]
	v_cvt_f64_f32_e32 v[84:85], v83
	v_or_b32_e32 v81, 32, v40
	v_or_b32_e32 v82, 33, v41
	v_min_u32_e32 v80, v81, v82
	v_or_b32_e32 v81, 34, v42
	v_or_b32_e32 v82, 35, v43
	v_min3_u32 v80, v80, v81, v82
	v_or_b32_e32 v81, 36, v44
	v_or_b32_e32 v82, 37, v45
	v_min3_u32 v80, v80, v81, v82
	v_or_b32_e32 v81, 38, v46
	v_or_b32_e32 v82, 39, v47
	v_min3_u32 v80, v80, v81, v82
	v_or_b32_e32 v81, 40, v48
	v_or_b32_e32 v82, 41, v49
	v_min3_u32 v80, v80, v81, v82
	v_or_b32_e32 v81, 42, v50
	v_or_b32_e32 v82, 43, v51
	v_min3_u32 v80, v80, v81, v82
	v_or_b32_e32 v81, 44, v52
	v_or_b32_e32 v82, 45, v53
	v_min3_u32 v80, v80, v81, v82
	v_or_b32_e32 v81, 46, v54
	v_or_b32_e32 v82, 47, v55
	v_min3_u32 v80, v80, v81, v82
	v_mul_f64 v[86:87], v[86:87], v[84:85]
	v_pk_mul_f32 v[40:41], v[40:41], s[14:15] op_sel_hi:[1,0]
	v_pk_mul_f32 v[42:43], v[42:43], s[14:15] op_sel_hi:[1,0]
	v_pk_mul_f32 v[44:45], v[44:45], s[14:15] op_sel_hi:[1,0]
	v_pk_mul_f32 v[46:47], v[46:47], s[14:15] op_sel_hi:[1,0]
	v_pk_mul_f32 v[48:49], v[48:49], s[14:15] op_sel_hi:[1,0]
	v_pk_mul_f32 v[50:51], v[50:51], s[14:15] op_sel_hi:[1,0]
	v_pk_mul_f32 v[52:53], v[52:53], s[14:15] op_sel_hi:[1,0]
	v_pk_mul_f32 v[54:55], v[54:55], s[14:15] op_sel_hi:[1,0]
	v_exp_f32_e32 v40, v40
	v_exp_f32_e32 v41, v41
	v_exp_f32_e32 v42, v42
	v_exp_f32_e32 v43, v43
	v_exp_f32_e32 v44, v44
	v_exp_f32_e32 v45, v45
	v_exp_f32_e32 v46, v46
	v_exp_f32_e32 v47, v47
	v_exp_f32_e32 v48, v48
	v_exp_f32_e32 v49, v49
	v_exp_f32_e32 v50, v50
	v_exp_f32_e32 v51, v51
	v_exp_f32_e32 v52, v52
	v_exp_f32_e32 v53, v53
	v_exp_f32_e32 v54, v54
	v_exp_f32_e32 v55, v55
	v_pk_add_f32 v[78:79], v[40:41], v[42:43]
	v_pk_add_f32 v[78:79], v[78:79], v[44:45]
	v_pk_add_f32 v[78:79], v[78:79], v[46:47]
	v_pk_add_f32 v[78:79], v[78:79], v[48:49]
	v_pk_add_f32 v[78:79], v[78:79], v[50:51]
	v_pk_add_f32 v[78:79], v[78:79], v[52:53]
	v_pk_add_f32 v[78:79], v[78:79], v[54:55]
	v_add_f32_e32 v78, v78, v79
	v_cvt_f64_f32_e32 v[84:85], v78
	v_cndmask_b32_e64 v75, v75, v80, s[26:27]
	v_mov_b32_e32 v73, v100
	v_add_f64 v[86:87], v[86:87], v[84:85]
	s_waitcnt vmcnt(9)
	v_max3_f32 v76, v56, v57, v58
	v_max3_f32 v76, v76, v59, v60
	v_max3_f32 v76, v76, v61, v62
	v_max_f32_e32 v76, v76, v63
	v_max_f32_e32 v100, v73, v76
	v_cmp_gt_f32_e64 s[26:27], v76, v73
	v_sub_f32_e32 v83, v73, v100
	v_mul_f32_e32 v83, s14, v83
	v_exp_f32_e32 v83, v83
	v_pk_add_f32 v[56:57], v[56:57], v[100:101] op_sel_hi:[1,0] neg_lo:[0,1] neg_hi:[0,1]
	v_pk_add_f32 v[58:59], v[58:59], v[100:101] op_sel_hi:[1,0] neg_lo:[0,1] neg_hi:[0,1]
	v_pk_add_f32 v[60:61], v[60:61], v[100:101] op_sel_hi:[1,0] neg_lo:[0,1] neg_hi:[0,1]
	v_pk_add_f32 v[62:63], v[62:63], v[100:101] op_sel_hi:[1,0] neg_lo:[0,1] neg_hi:[0,1]
	v_cvt_f64_f32_e32 v[84:85], v83
	v_or_b32_e32 v81, 48, v56
	v_or_b32_e32 v82, 49, v57
	v_min_u32_e32 v80, v81, v82
	v_or_b32_e32 v81, 50, v58
	v_or_b32_e32 v82, 51, v59
	v_min3_u32 v80, v80, v81, v82
	v_or_b32_e32 v81, 52, v60
	v_or_b32_e32 v82, 53, v61
	v_min3_u32 v80, v80, v81, v82
	v_or_b32_e32 v81, 54, v62
	v_or_b32_e32 v82, 55, v63
	v_min3_u32 v80, v80, v81, v82
	v_mul_f64 v[86:87], v[86:87], v[84:85]
	v_pk_mul_f32 v[56:57], v[56:57], s[14:15] op_sel_hi:[1,0]
	v_pk_mul_f32 v[58:59], v[58:59], s[14:15] op_sel_hi:[1,0]
	v_pk_mul_f32 v[60:61], v[60:61], s[14:15] op_sel_hi:[1,0]
	v_pk_mul_f32 v[62:63], v[62:63], s[14:15] op_sel_hi:[1,0]
	v_exp_f32_e32 v56, v56
	v_exp_f32_e32 v57, v57
	v_exp_f32_e32 v58, v58
	v_exp_f32_e32 v59, v59
	v_exp_f32_e32 v60, v60
	v_exp_f32_e32 v61, v61
	v_exp_f32_e32 v62, v62
	v_exp_f32_e32 v63, v63
	v_pk_add_f32 v[78:79], v[56:57], v[58:59]
	v_pk_add_f32 v[78:79], v[78:79], v[60:61]
	v_pk_add_f32 v[78:79], v[78:79], v[62:63]
	v_add_f32_e32 v78, v78, v79
	v_cvt_f64_f32_e32 v[84:85], v78
	v_cndmask_b32_e64 v75, v75, v80, s[26:27]
	v_mov_b32_e32 v73, v100
	v_add_f64 v[86:87], v[86:87], v[84:85]
	s_waitcnt vmcnt(5)
	v_max3_f32 v76, v64, v65, v66
	v_max_f32_e32 v76, v76, v67
	v_max_f32_e32 v100, v73, v76
	v_cmp_gt_f32_e64 s[26:27], v76, v73
	v_sub_f32_e32 v83, v73, v100
	v_mul_f32_e32 v83, s14, v83
	v_exp_f32_e32 v83, v83
	v_pk_add_f32 v[64:65], v[64:65], v[100:101] op_sel_hi:[1,0] neg_lo:[0,1] neg_hi:[0,1]
	v_pk_add_f32 v[66:67], v[66:67], v[100:101] op_sel_hi:[1,0] neg_lo:[0,1] neg_hi:[0,1]
	v_cvt_f64_f32_e32 v[84:85], v83
	v_or_b32_e32 v81, 56, v64
	v_or_b32_e32 v82, 57, v65
	v_min_u32_e32 v80, v81, v82
	v_or_b32_e32 v81, 58, v66
	v_or_b32_e32 v82, 59, v67
	v_min3_u32 v80, v80, v81, v82
	v_mul_f64 v[86:87], v[86:87], v[84:85]
	v_pk_mul_f32 v[64:65], v[64:65], s[14:15] op_sel_hi:[1,0]
	v_pk_mul_f32 v[66:67], v[66:67], s[14:15] op_sel_hi:[1,0]
	v_exp_f32_e32 v64, v64
	v_exp_f32_e32 v65, v65
	v_exp_f32_e32 v66, v66
	v_exp_f32_e32 v67, v67
	s_nop 0
	v_pk_add_f32 v[78:79], v[64:65], v[66:67]
	v_add_f32_e32 v78, v78, v79
	v_cvt_f64_f32_e32 v[84:85], v78
	v_cndmask_b32_e64 v75, v75, v80, s[26:27]
	v_mov_b32_e32 v73, v100
	v_add_f64 v[86:87], v[86:87], v[84:85]
	s_waitcnt vmcnt(4)
	v_max_f32_e32 v100, v73, v68
	v_cmp_gt_f32_e64 s[26:27], v68, v73
	v_sub_f32_e32 v83, v73, v100
	v_sub_f32_e32 v68, v68, v100
	v_mul_f32_e32 v83, s14, v83
	v_mul_f32_e32 v68, s14, v68
	v_exp_f32_e32 v83, v83
	v_exp_f32_e32 v68, v68
	v_cndmask_b32_e64 v75, v75, 60, s[26:27]
	v_cvt_f64_f32_e32 v[84:85], v83
	v_cvt_f64_f32_e32 v[90:91], v68
	v_mul_f64 v[86:87], v[86:87], v[84:85]
	v_mov_b32_e32 v73, v100
	v_add_f64 v[86:87], v[86:87], v[90:91]
	s_waitcnt vmcnt(3)
	v_max_f32_e32 v100, v73, v69
	v_cmp_gt_f32_e64 s[26:27], v69, v73
	v_sub_f32_e32 v83, v73, v100
	v_sub_f32_e32 v69, v69, v100
	v_mul_f32_e32 v83, s14, v83
	v_mul_f32_e32 v69, s14, v69
	v_exp_f32_e32 v83, v83
	v_exp_f32_e32 v69, v69
	v_cndmask_b32_e64 v75, v75, 61, s[26:27]
	v_cvt_f64_f32_e32 v[84:85], v83
	v_cvt_f64_f32_e32 v[90:91], v69
	v_mul_f64 v[86:87], v[86:87], v[84:85]
	v_mov_b32_e32 v73, v100
	v_add_f64 v[86:87], v[86:87], v[90:91]
	s_waitcnt vmcnt(2)
	v_max_f32_e32 v100, v73, v70
	v_cmp_gt_f32_e64 s[26:27], v70, v73
	v_sub_f32_e32 v83, v73, v100
	v_sub_f32_e32 v70, v70, v100
	v_mul_f32_e32 v83, s14, v83
	v_mul_f32_e32 v70, s14, v70
	v_exp_f32_e32 v83, v83
	v_exp_f32_e32 v70, v70
	v_cndmask_b32_e64 v75, v75, 62, s[26:27]
	v_cvt_f64_f32_e32 v[84:85], v83
	v_cvt_f64_f32_e32 v[90:91], v70
	v_mul_f64 v[86:87], v[86:87], v[84:85]
	v_mov_b32_e32 v73, v100
	v_add_f64 v[86:87], v[86:87], v[90:91]
	s_waitcnt vmcnt(1)
	v_max_f32_e32 v100, v73, v71
	v_cmp_gt_f32_e64 s[26:27], v71, v73
	v_sub_f32_e32 v83, v73, v100
	v_sub_f32_e32 v71, v71, v100
	v_mul_f32_e32 v83, s14, v83
	v_mul_f32_e32 v71, s14, v71
	v_exp_f32_e32 v83, v83
	v_exp_f32_e32 v71, v71
	v_cndmask_b32_e64 v75, v75, 63, s[26:27]
	v_cvt_f64_f32_e32 v[84:85], v83
	v_cvt_f64_f32_e32 v[90:91], v71
	v_mul_f64 v[86:87], v[86:87], v[84:85]
	v_mov_b32_e32 v73, v100
	v_add_f64 v[86:87], v[86:87], v[90:91]
	s_waitcnt vmcnt(0)
	v_max_f32_e32 v100, v73, v72
	v_cmp_gt_f32_e64 s[26:27], v72, v73
	v_sub_f32_e32 v83, v73, v100
	v_sub_f32_e32 v72, v72, v100
	v_mul_f32_e32 v83, s14, v83
	v_mul_f32_e32 v72, s14, v72
	v_exp_f32_e32 v83, v83
	v_exp_f32_e32 v72, v72
	v_cndmask_b32_e64 v75, v75, 64, s[26:27]
	v_cvt_f64_f32_e32 v[84:85], v83
	v_cvt_f64_f32_e32 v[90:91], v72
	v_mul_f64 v[86:87], v[86:87], v[84:85]
	v_add_f64 v[86:87], v[86:87], v[90:91]
	v_rcp_f64_e32 v[88:89], v[86:87]
	v_cmp_gt_u32_e32 vcc, 64, v75
	s_and_b64 vcc, vcc, s[36:37]
	v_fma_f64 v[90:91], -v[86:87], v[88:89], 1.0
	v_fma_f64 v[88:89], v[90:91], v[88:89], v[88:89]
	v_cvt_f32_f64_e32 v3, v[88:89]
	v_cndmask_b32_e32 v74, 0, v3, vcc
	global_store_dwordx2 v98, v[74:75], s[6:7]

	.amdhsa_kernel _Z12score_kernelPKfP15HIP_vector_typeIjLj2EES0_S0_
		.amdhsa_group_segment_fixed_size 0
		.amdhsa_private_segment_fixed_size 0
		.amdhsa_kernarg_size 32
		.amdhsa_user_sgpr_count 2
		.amdhsa_user_sgpr_dispatch_ptr 0
		.amdhsa_user_sgpr_queue_ptr 0
		.amdhsa_user_sgpr_kernarg_segment_ptr 1
		.amdhsa_user_sgpr_dispatch_id 0
		.amdhsa_user_sgpr_kernarg_preload_length 0
		.amdhsa_user_sgpr_kernarg_preload_offset 0
		.amdhsa_user_sgpr_private_segment_size 0
		.amdhsa_uses_dynamic_stack 0
		.amdhsa_enable_private_segment 0
		.amdhsa_system_sgpr_workgroup_id_x 1
		.amdhsa_system_sgpr_workgroup_id_y 0
		.amdhsa_system_sgpr_workgroup_id_z 0
		.amdhsa_system_sgpr_workgroup_info 0
		.amdhsa_system_vgpr_workitem_id 0
		.amdhsa_next_free_vgpr 102
		.amdhsa_next_free_sgpr 56
		.amdhsa_accum_offset 104
		.amdhsa_reserve_vcc 1
		.amdhsa_float_round_mode_32 0
		.amdhsa_float_round_mode_16_64 0
		.amdhsa_float_denorm_mode_32 3
		.amdhsa_float_denorm_mode_16_64 3
		.amdhsa_dx10_clamp 1
		.amdhsa_ieee_mode 1
		.amdhsa_fp16_overflow 0
		.amdhsa_tg_split 0
		.amdhsa_exception_fp_ieee_invalid_op 0
		.amdhsa_exception_fp_denorm_src 0
		.amdhsa_exception_fp_ieee_div_zero 0
		.amdhsa_exception_fp_ieee_overflow 0
		.amdhsa_exception_fp_ieee_underflow 0
		.amdhsa_exception_fp_ieee_inexact 0
		.amdhsa_exception_int_div_zero 0
	.end_amdhsa_kernel

amdhsa.kernels:
  - .agpr_count:     0
    .args:
      - .actual_access:  read_only
        .address_space:  global
        .offset:         0
        .size:           8
        .value_kind:     global_buffer
      - .actual_access:  write_only
        .address_space:  global
        .offset:         8
        .size:           8
        .value_kind:     global_buffer
      - .actual_access:  read_only
        .address_space:  global
        .offset:         16
        .size:           8
        .value_kind:     global_buffer
      - .actual_access:  read_only
        .address_space:  global
        .offset:         24
        .size:           8
        .value_kind:     global_buffer
    .group_segment_fixed_size: 0
    .kernarg_segment_align: 8
    .kernarg_segment_size: 32
    .language:       OpenCL C
    .language_version:
      - 2
      - 0
    .max_flat_workgroup_size: 640
    .name:           _Z12score_kernelPKfP15HIP_vector_typeIjLj2EES0_S0_
    .private_segment_fixed_size: 0
    .sgpr_count:     62
    .sgpr_spill_count: 0
    .symbol:         _Z12score_kernelPKfP15HIP_vector_typeIjLj2EES0_S0_.kd
    .uniform_work_group_size: 1
    .uses_dynamic_stack: false
    .vgpr_count:     102
    .vgpr_spill_count: 0
    .wavefront_size: 64
  - .agpr_count:     0
    .args:
      - .actual_access:  read_only
        .address_space:  global
        .offset:         0
        .size:           8
        .value_kind:     global_buffer
      - .actual_access:  read_only
        .address_space:  global
        .offset:         8
        .size:           8
        .value_kind:     global_buffer
      - .actual_access:  write_only
        .address_space:  global
        .offset:         16
        .size:           8
        .value_kind:     global_buffer
    .group_segment_fixed_size: 49664
    .kernarg_segment_align: 8
    .kernarg_segment_size: 24
    .language:       OpenCL C
    .language_version:
      - 2
      - 0
    .max_flat_workgroup_size: 1024
    .name:           _Z13select_kernelPK15HIP_vector_typeIjLj2EEPKfPf
    .private_segment_fixed_size: 0
    .sgpr_count:     58
    .sgpr_spill_count: 0
    .symbol:         _Z13select_kernelPK15HIP_vector_typeIjLj2EEPKfPf.kd
    .uniform_work_group_size: 1
    .uses_dynamic_stack: false
    .vgpr_count:     63
    .vgpr_spill_count: 0
    .wavefront_size: 64
